# RG unit prologue (both passes): eight predicated x-tile loads issued back to back on private registers (were load -> vmcnt(0) -> ds_write each), plus the output-gating load hoist
# speedup vs baseline: 1.0064x; 1.0064x over previous
.LBB0_371:
	s_mul_hi_i32 s2, s6, 0x3e0f83e1
	s_lshr_b32 s3, s2, 31
	s_ashr_i32 s4, s2, 5
	s_add_i32 s4, s4, s3
	s_mul_i32 s5, s4, 0x84
	s_sub_i32 s7, s6, s5
	s_lshl_b32 s2, s4, 8
	s_lshl_b32 s10, s7, 6
	s_add_i32 s2, s2, 0x10000
	s_lshl_b32 s3, s4, 13
	s_add_i32 s11, s10, 0xffffff00
	s_cmp_lt_i32 s7, 4
	s_cselect_b32 s10, s10, s11
	s_cselect_b32 s9, s31, 0x2000
	s_cselect_b32 s8, s2, s3
	s_add_i32 s10, s10, -2
	v_mov_b32_e32 v8, 0
	v_add_u32_e32 v9, s10, v71
	v_cmp_gt_u32_e32 vcc, s9, v9
	v_mov_b32_e32 v8, 0
	v_lshlrev_b32_e32 v0, 1, v70
	v_mov_b32_e32 v10, 0
	v_mov_b32_e32 v11, 0
	v_mov_b32_e32 v12, 0
	v_mov_b32_e32 v13, 0
	s_and_saveexec_b64 s[2:3], vcc
	s_cbranch_execz .LBB0_373
	v_add_u32_e32 v9, s8, v9
	v_mov_b64_e32 v[10:11], s[0:1]
	s_movk_i32 s11, 0x2c00
	v_mad_i64_i32 v[10:11], s[12:13], v9, s11, v[10:11]
	s_lshl_b32 s14, s28, 1
	v_lshl_add_u64 v[10:11], v[10:11], 0, s[14:15]
	v_lshl_add_u64 v[10:11], v[10:11], 0, v[0:1]
	v_add_co_u32_e32 v10, vcc, 0x1000, v10
	s_nop 1
	v_addc_co_u32_e32 v11, vcc, 0, v11, vcc
	global_load_dwordx4 v[10:13], v[10:11], off offset:1024
.LBB0_373:
	s_or_b64 exec, exec, s[2:3]
	v_mov_b32_e32 v14, 0
	v_add_u32_e32 v18, s10, v74
	v_cmp_gt_u32_e32 vcc, s9, v18
	v_mov_b32_e32 v15, 0
	v_mov_b32_e32 v16, 0
	v_mov_b32_e32 v17, 0
	s_and_saveexec_b64 s[2:3], vcc
	s_cbranch_execz .LBB0_375
	v_add_u32_e32 v16, s8, v18
	v_mov_b64_e32 v[14:15], s[0:1]
	s_movk_i32 s11, 0x2c00
	v_mad_i64_i32 v[14:15], s[12:13], v16, s11, v[14:15]
	s_lshl_b32 s14, s28, 1
	v_lshl_add_u64 v[14:15], v[14:15], 0, s[14:15]
	v_lshl_add_u64 v[14:15], v[14:15], 0, v[0:1]
	v_add_co_u32_e32 v14, vcc, 0x1000, v14
	s_nop 1
	v_addc_co_u32_e32 v15, vcc, 0, v15, vcc
	global_load_dwordx4 v[14:17], v[14:15], off offset:1024
.LBB0_375:
	s_or_b64 exec, exec, s[2:3]
	v_mov_b32_e32 v20, 0
	v_add_u32_e32 v21, s10, v75
	v_cmp_gt_u32_e32 vcc, s9, v21
	v_mov_b32_e32 v20, 0
	v_mov_b32_e32 v22, 0
	v_mov_b32_e32 v23, 0
	v_mov_b32_e32 v24, 0
	v_mov_b32_e32 v25, 0
	s_and_saveexec_b64 s[2:3], vcc
	s_cbranch_execz .LBB0_377
	v_add_u32_e32 v21, s8, v21
	v_mov_b64_e32 v[22:23], s[0:1]
	s_movk_i32 s11, 0x2c00
	v_mad_i64_i32 v[22:23], s[12:13], v21, s11, v[22:23]
	s_lshl_b32 s14, s28, 1
	v_lshl_add_u64 v[22:23], v[22:23], 0, s[14:15]
	v_lshl_add_u64 v[22:23], v[22:23], 0, v[0:1]
	v_add_co_u32_e32 v22, vcc, 0x1000, v22
	s_nop 1
	v_addc_co_u32_e32 v23, vcc, 0, v23, vcc
	global_load_dwordx4 v[22:25], v[22:23], off offset:1024
.LBB0_377:
	s_or_b64 exec, exec, s[2:3]
	v_mov_b32_e32 v26, 0
	v_add_u32_e32 v30, s10, v76
	v_cmp_gt_u32_e32 vcc, s9, v30
	v_mov_b32_e32 v27, 0
	v_mov_b32_e32 v28, 0
	v_mov_b32_e32 v29, 0
	s_and_saveexec_b64 s[2:3], vcc
	s_cbranch_execz .LBB0_379
	v_add_u32_e32 v28, s8, v30
	v_mov_b64_e32 v[26:27], s[0:1]
	s_movk_i32 s11, 0x2c00
	v_mad_i64_i32 v[26:27], s[12:13], v28, s11, v[26:27]
	s_lshl_b32 s14, s28, 1
	v_lshl_add_u64 v[26:27], v[26:27], 0, s[14:15]
	v_lshl_add_u64 v[26:27], v[26:27], 0, v[0:1]
	v_add_co_u32_e32 v26, vcc, 0x1000, v26
	s_nop 1
	v_addc_co_u32_e32 v27, vcc, 0, v27, vcc
	global_load_dwordx4 v[26:29], v[26:27], off offset:1024
.LBB0_379:
	s_or_b64 exec, exec, s[2:3]
	v_mov_b32_e32 v32, 0
	v_add_u32_e32 v33, s10, v77
	v_cmp_gt_u32_e32 vcc, s9, v33
	v_mov_b32_e32 v32, 0
	v_mov_b32_e32 v34, 0
	v_mov_b32_e32 v35, 0
	v_mov_b32_e32 v36, 0
	v_mov_b32_e32 v37, 0
	s_and_saveexec_b64 s[2:3], vcc
	s_cbranch_execz .LBB0_381
	v_add_u32_e32 v33, s8, v33
	v_mov_b64_e32 v[34:35], s[0:1]
	s_movk_i32 s11, 0x2c00
	v_mad_i64_i32 v[34:35], s[12:13], v33, s11, v[34:35]
	s_lshl_b32 s14, s28, 1
	v_lshl_add_u64 v[34:35], v[34:35], 0, s[14:15]
	v_lshl_add_u64 v[34:35], v[34:35], 0, v[0:1]
	v_add_co_u32_e32 v34, vcc, 0x1000, v34
	s_nop 1
	v_addc_co_u32_e32 v35, vcc, 0, v35, vcc
	global_load_dwordx4 v[34:37], v[34:35], off offset:1024
.LBB0_381:
	s_or_b64 exec, exec, s[2:3]
	v_mov_b32_e32 v38, 0
	v_add_u32_e32 v42, s10, v78
	v_cmp_gt_u32_e32 vcc, s9, v42
	v_mov_b32_e32 v39, 0
	v_mov_b32_e32 v40, 0
	v_mov_b32_e32 v41, 0
	s_and_saveexec_b64 s[2:3], vcc
	s_cbranch_execz .LBB0_383
	v_add_u32_e32 v40, s8, v42
	v_mov_b64_e32 v[38:39], s[0:1]
	s_movk_i32 s11, 0x2c00
	v_mad_i64_i32 v[38:39], s[12:13], v40, s11, v[38:39]
	s_lshl_b32 s14, s28, 1
	v_lshl_add_u64 v[38:39], v[38:39], 0, s[14:15]
	v_lshl_add_u64 v[38:39], v[38:39], 0, v[0:1]
	v_add_co_u32_e32 v38, vcc, 0x1000, v38
	s_nop 1
	v_addc_co_u32_e32 v39, vcc, 0, v39, vcc
	global_load_dwordx4 v[38:41], v[38:39], off offset:1024
.LBB0_383:
	s_or_b64 exec, exec, s[2:3]
	v_mov_b32_e32 v44, 0
	v_add_u32_e32 v45, s10, v79
	v_cmp_gt_u32_e32 vcc, s9, v45
	v_mov_b32_e32 v44, 0
	v_mov_b32_e32 v46, 0
	v_mov_b32_e32 v47, 0
	v_mov_b32_e32 v48, 0
	v_mov_b32_e32 v49, 0
	s_and_saveexec_b64 s[2:3], vcc
	s_cbranch_execz .LBB0_385
	v_add_u32_e32 v45, s8, v45
	v_mov_b64_e32 v[46:47], s[0:1]
	s_movk_i32 s11, 0x2c00
	v_mad_i64_i32 v[46:47], s[12:13], v45, s11, v[46:47]
	s_lshl_b32 s14, s28, 1
	v_lshl_add_u64 v[46:47], v[46:47], 0, s[14:15]
	v_lshl_add_u64 v[46:47], v[46:47], 0, v[0:1]
	v_add_co_u32_e32 v46, vcc, 0x1000, v46
	s_nop 1
	v_addc_co_u32_e32 v47, vcc, 0, v47, vcc
	global_load_dwordx4 v[46:49], v[46:47], off offset:1024
.LBB0_385:
	s_or_b64 exec, exec, s[2:3]
	v_mov_b32_e32 v2, 0
	v_add_u32_e32 v6, s10, v80
	v_cmp_gt_u32_e32 vcc, s9, v6
	v_mov_b32_e32 v3, 0
	v_mov_b32_e32 v4, 0
	v_mov_b32_e32 v5, 0
	s_and_saveexec_b64 s[2:3], vcc
	s_cbranch_execz .LBB0_387
	v_add_u32_e32 v4, s8, v6
	v_mov_b64_e32 v[2:3], s[0:1]
	s_movk_i32 s11, 0x2c00
	v_mad_i64_i32 v[2:3], s[12:13], v4, s11, v[2:3]
	s_lshl_b32 s14, s28, 1
	v_lshl_add_u64 v[2:3], v[2:3], 0, s[14:15]
	v_lshl_add_u64 v[2:3], v[2:3], 0, v[0:1]
	v_add_co_u32_e32 v2, vcc, 0x1000, v2
	s_nop 1
	v_addc_co_u32_e32 v3, vcc, 0, v3, vcc
	global_load_dwordx4 v[2:5], v[2:3], off offset:1024
.LBB0_387:
	s_or_b64 exec, exec, s[2:3]
	v_add_u32_e32 v6, s10, v81
	v_cmp_gt_u32_e32 vcc, s9, v6
	s_waitcnt vmcnt(0)
	ds_write_b128 v95, v[2:5] offset:8064
	ds_write_b128 v95, v[10:13]
	ds_write_b128 v95, v[14:17] offset:1152
	ds_write_b128 v95, v[22:25] offset:2304
	ds_write_b128 v95, v[26:29] offset:3456
	ds_write_b128 v95, v[34:37] offset:4608
	ds_write_b128 v95, v[38:41] offset:5760
	ds_write_b128 v95, v[46:49] offset:6912
	s_and_b64 s[10:11], s[38:39], vcc
	v_mov_b32_e32 v2, 0
	v_mov_b32_e32 v3, 0
	v_mov_b32_e32 v4, 0
	v_mov_b32_e32 v5, 0
	s_and_saveexec_b64 s[2:3], s[10:11]
	s_cbranch_execz .LBB0_389
	v_add_u32_e32 v4, s8, v6
	v_mov_b64_e32 v[2:3], s[0:1]
	s_movk_i32 s8, 0x2c00
	v_mad_i64_i32 v[2:3], s[8:9], v4, s8, v[2:3]
	s_lshl_b32 s14, s28, 1
	v_lshl_add_u64 v[2:3], v[2:3], 0, s[14:15]
	v_lshl_add_u64 v[2:3], v[2:3], 0, v[0:1]
	v_add_co_u32_e32 v2, vcc, 0x1000, v2
	s_nop 1
	v_addc_co_u32_e32 v3, vcc, 0, v3, vcc
	global_load_dwordx4 v[2:5], v[2:3], off offset:1024

.LBB0_600:
	s_abs_i32 s5, s11
	s_mul_hi_u32 s8, s5, s12
	s_mul_i32 s9, s8, s7
	s_sub_i32 s5, s5, s9
	s_ashr_i32 s4, s11, 31
	s_add_i32 s9, s8, 1
	s_sub_i32 s13, s5, s7
	s_cmp_ge_u32 s5, s7
	s_cselect_b32 s8, s9, s8
	s_cselect_b32 s5, s13, s5
	s_add_i32 s9, s8, 1
	s_cmp_ge_u32 s5, s7
	s_cselect_b32 s5, s9, s8
	s_xor_b32 s5, s5, s4
	s_sub_i32 s13, s5, s4
	s_mul_i32 s4, s13, s7
	s_sub_i32 s16, s11, s4
	s_add_i32 s16, s16, s6
	s_lshl_b32 s4, s13, 8
	s_lshl_b32 s9, s16, 6
	s_add_i32 s4, s4, 0x10000
	s_lshl_b32 s5, s13, 13
	s_add_i32 s18, s9, 0xffffff00
	s_cmp_lt_i32 s16, 4
	s_cselect_b32 s9, s9, s18
	s_cselect_b32 s17, s33, 0x2000
	s_cselect_b32 s8, s4, s5
	s_add_i32 s18, s9, -2
	v_mov_b32_e32 v8, 0
	v_add_u32_e32 v9, s18, v71
	v_cmp_gt_u32_e32 vcc, s17, v9
	v_mov_b32_e32 v8, 0
	v_lshlrev_b32_e32 v0, 1, v70
	v_mov_b32_e32 v10, 0
	v_mov_b32_e32 v11, 0
	v_mov_b32_e32 v12, 0
	v_mov_b32_e32 v13, 0
	s_and_saveexec_b64 s[4:5], vcc
	s_cbranch_execz .LBB0_602
	v_add_u32_e32 v9, s8, v9
	v_mov_b64_e32 v[10:11], s[2:3]
	s_movk_i32 s19, 0x2c00
	v_mad_i64_i32 v[10:11], s[20:21], v9, s19, v[10:11]
	v_lshl_add_u64 v[10:11], v[10:11], 0, s[14:15]
	v_lshl_add_u64 v[10:11], v[10:11], 0, v[0:1]
	v_add_co_u32_e32 v10, vcc, 0x1000, v10
	s_nop 1
	v_addc_co_u32_e32 v11, vcc, 0, v11, vcc
	global_load_dwordx4 v[10:13], v[10:11], off offset:1024
.LBB0_602:
	s_or_b64 exec, exec, s[4:5]
	v_mov_b32_e32 v14, 0
	v_add_u32_e32 v18, s18, v79
	v_cmp_gt_u32_e32 vcc, s17, v18
	v_mov_b32_e32 v15, 0
	v_mov_b32_e32 v16, 0
	v_mov_b32_e32 v17, 0
	s_and_saveexec_b64 s[4:5], vcc
	s_cbranch_execz .LBB0_604
	v_add_u32_e32 v16, s8, v18
	v_mov_b64_e32 v[14:15], s[2:3]
	s_movk_i32 s19, 0x2c00
	v_mad_i64_i32 v[14:15], s[20:21], v16, s19, v[14:15]
	v_lshl_add_u64 v[14:15], v[14:15], 0, s[14:15]
	v_lshl_add_u64 v[14:15], v[14:15], 0, v[0:1]
	v_add_co_u32_e32 v14, vcc, 0x1000, v14
	s_nop 1
	v_addc_co_u32_e32 v15, vcc, 0, v15, vcc
	global_load_dwordx4 v[14:17], v[14:15], off offset:1024
.LBB0_604:
	s_or_b64 exec, exec, s[4:5]
	v_mov_b32_e32 v20, 0
	v_add_u32_e32 v21, s18, v81
	v_cmp_gt_u32_e32 vcc, s17, v21
	v_mov_b32_e32 v20, 0
	v_mov_b32_e32 v22, 0
	v_mov_b32_e32 v23, 0
	v_mov_b32_e32 v24, 0
	v_mov_b32_e32 v25, 0
	s_and_saveexec_b64 s[4:5], vcc
	s_cbranch_execz .LBB0_606
	v_add_u32_e32 v21, s8, v21
	v_mov_b64_e32 v[22:23], s[2:3]
	s_movk_i32 s19, 0x2c00
	v_mad_i64_i32 v[22:23], s[20:21], v21, s19, v[22:23]
	v_lshl_add_u64 v[22:23], v[22:23], 0, s[14:15]
	v_lshl_add_u64 v[22:23], v[22:23], 0, v[0:1]
	v_add_co_u32_e32 v22, vcc, 0x1000, v22
	s_nop 1
	v_addc_co_u32_e32 v23, vcc, 0, v23, vcc
	global_load_dwordx4 v[22:25], v[22:23], off offset:1024
.LBB0_606:
	s_or_b64 exec, exec, s[4:5]
	v_mov_b32_e32 v26, 0
	v_add_u32_e32 v30, s18, v83
	v_cmp_gt_u32_e32 vcc, s17, v30
	v_mov_b32_e32 v27, 0
	v_mov_b32_e32 v28, 0
	v_mov_b32_e32 v29, 0
	s_and_saveexec_b64 s[4:5], vcc
	s_cbranch_execz .LBB0_608
	v_add_u32_e32 v28, s8, v30
	v_mov_b64_e32 v[26:27], s[2:3]
	s_movk_i32 s19, 0x2c00
	v_mad_i64_i32 v[26:27], s[20:21], v28, s19, v[26:27]
	v_lshl_add_u64 v[26:27], v[26:27], 0, s[14:15]
	v_lshl_add_u64 v[26:27], v[26:27], 0, v[0:1]
	v_add_co_u32_e32 v26, vcc, 0x1000, v26
	s_nop 1
	v_addc_co_u32_e32 v27, vcc, 0, v27, vcc
	global_load_dwordx4 v[26:29], v[26:27], off offset:1024
.LBB0_608:
	s_or_b64 exec, exec, s[4:5]
	v_mov_b32_e32 v32, 0
	v_add_u32_e32 v33, s18, v85
	v_cmp_gt_u32_e32 vcc, s17, v33
	v_mov_b32_e32 v32, 0
	v_mov_b32_e32 v34, 0
	v_mov_b32_e32 v35, 0
	v_mov_b32_e32 v36, 0
	v_mov_b32_e32 v37, 0
	s_and_saveexec_b64 s[4:5], vcc
	s_cbranch_execz .LBB0_610
	v_add_u32_e32 v33, s8, v33
	v_mov_b64_e32 v[34:35], s[2:3]
	s_movk_i32 s19, 0x2c00
	v_mad_i64_i32 v[34:35], s[20:21], v33, s19, v[34:35]
	v_lshl_add_u64 v[34:35], v[34:35], 0, s[14:15]
	v_lshl_add_u64 v[34:35], v[34:35], 0, v[0:1]
	v_add_co_u32_e32 v34, vcc, 0x1000, v34
	s_nop 1
	v_addc_co_u32_e32 v35, vcc, 0, v35, vcc
	global_load_dwordx4 v[34:37], v[34:35], off offset:1024
.LBB0_610:
	s_or_b64 exec, exec, s[4:5]
	v_mov_b32_e32 v38, 0
	v_add_u32_e32 v42, s18, v87
	v_cmp_gt_u32_e32 vcc, s17, v42
	v_mov_b32_e32 v39, 0
	v_mov_b32_e32 v40, 0
	v_mov_b32_e32 v41, 0
	s_and_saveexec_b64 s[4:5], vcc
	s_cbranch_execz .LBB0_612
	v_add_u32_e32 v40, s8, v42
	v_mov_b64_e32 v[38:39], s[2:3]
	s_movk_i32 s19, 0x2c00
	v_mad_i64_i32 v[38:39], s[20:21], v40, s19, v[38:39]
	v_lshl_add_u64 v[38:39], v[38:39], 0, s[14:15]
	v_lshl_add_u64 v[38:39], v[38:39], 0, v[0:1]
	v_add_co_u32_e32 v38, vcc, 0x1000, v38
	s_nop 1
	v_addc_co_u32_e32 v39, vcc, 0, v39, vcc
	global_load_dwordx4 v[38:41], v[38:39], off offset:1024
.LBB0_612:
	s_or_b64 exec, exec, s[4:5]
	v_mov_b32_e32 v44, 0
	v_add_u32_e32 v45, s18, v89
	v_cmp_gt_u32_e32 vcc, s17, v45
	v_mov_b32_e32 v44, 0
	v_mov_b32_e32 v46, 0
	v_mov_b32_e32 v47, 0
	v_mov_b32_e32 v48, 0
	v_mov_b32_e32 v49, 0
	s_and_saveexec_b64 s[4:5], vcc
	s_cbranch_execz .LBB0_614
	v_add_u32_e32 v45, s8, v45
	v_mov_b64_e32 v[46:47], s[2:3]
	s_movk_i32 s19, 0x2c00
	v_mad_i64_i32 v[46:47], s[20:21], v45, s19, v[46:47]
	v_lshl_add_u64 v[46:47], v[46:47], 0, s[14:15]
	v_lshl_add_u64 v[46:47], v[46:47], 0, v[0:1]
	v_add_co_u32_e32 v46, vcc, 0x1000, v46
	s_nop 1
	v_addc_co_u32_e32 v47, vcc, 0, v47, vcc
	global_load_dwordx4 v[46:49], v[46:47], off offset:1024
.LBB0_614:
	s_or_b64 exec, exec, s[4:5]
	v_mov_b32_e32 v2, 0
	v_add_u32_e32 v6, s18, v91
	v_cmp_gt_u32_e32 vcc, s17, v6
	v_mov_b32_e32 v3, 0
	v_mov_b32_e32 v4, 0
	v_mov_b32_e32 v5, 0
	s_and_saveexec_b64 s[4:5], vcc
	s_cbranch_execz .LBB0_616
	v_add_u32_e32 v4, s8, v6
	v_mov_b64_e32 v[2:3], s[2:3]
	s_movk_i32 s19, 0x2c00
	v_mad_i64_i32 v[2:3], s[20:21], v4, s19, v[2:3]
	v_lshl_add_u64 v[2:3], v[2:3], 0, s[14:15]
	v_lshl_add_u64 v[2:3], v[2:3], 0, v[0:1]
	v_add_co_u32_e32 v2, vcc, 0x1000, v2
	s_nop 1
	v_addc_co_u32_e32 v3, vcc, 0, v3, vcc
	global_load_dwordx4 v[2:5], v[2:3], off offset:1024
.LBB0_616:
	s_or_b64 exec, exec, s[4:5]
	v_add_u32_e32 v7, s18, v93
	v_add_u32_e32 v6, v78, v92
	v_cmp_gt_u32_e32 vcc, s17, v7
	s_waitcnt vmcnt(0)
	ds_write_b128 v6, v[2:5]
	ds_write_b128 v105, v[10:13]
	v_add_u32_e32 v18, v78, v80
	ds_write_b128 v18, v[14:17]
	v_add_u32_e32 v21, v78, v82
	ds_write_b128 v21, v[22:25]
	v_add_u32_e32 v30, v78, v84
	ds_write_b128 v30, v[26:29]
	v_add_u32_e32 v33, v78, v86
	ds_write_b128 v33, v[34:37]
	v_add_u32_e32 v42, v78, v88
	ds_write_b128 v42, v[38:41]
	v_add_u32_e32 v45, v78, v90
	ds_write_b128 v45, v[46:49]
	s_and_b64 s[18:19], s[38:39], vcc
	v_mov_b32_e32 v2, 0
	v_mov_b32_e32 v3, 0
	v_mov_b32_e32 v4, 0
	v_mov_b32_e32 v5, 0
	s_and_saveexec_b64 s[4:5], s[18:19]
	s_cbranch_execz .LBB0_618
	v_add_u32_e32 v4, s8, v7
	v_mov_b64_e32 v[2:3], s[2:3]
	s_movk_i32 s17, 0x2c00
	v_mad_i64_i32 v[2:3], s[18:19], v4, s17, v[2:3]
	v_lshl_add_u64 v[2:3], v[2:3], 0, s[14:15]
	v_lshl_add_u64 v[2:3], v[2:3], 0, v[0:1]
	v_add_co_u32_e32 v2, vcc, 0x1000, v2
	s_nop 1
	v_addc_co_u32_e32 v3, vcc, 0, v3, vcc
	global_load_dwordx4 v[2:5], v[2:3], off offset:1024
